# v28 plus conversion-tile re-deal in the fp8 phase tails (workgroups with one more GEMM unit take ~unit/6 tiles)
# speedup vs baseline: 1.0255x; 1.0058x over previous
; #define LAS __attribute__((address_space(3)))
; DI void cvt_group(const Params& p, LAS unsigned char* lds, int group, int t_lo, int t_hi, int r, int I) {
;     ...
;     __syncthreads();
;     const int nj = J[15].tile0, total = J[nj].tile0;
;     const int hi = min(t_hi, total);
;     const int row = tid >> 6, c4 = (tid & 63) * 4;
;     for (int gt = t_lo + r; gt < hi; gt += I) {
; DI void bg_range(const Params& p, LAS unsigned char* lds, int group, int t_lo, int t_hi, int nunits, int G, int bid) {
;     const int rem = nunits % G;
;     if (rem == 0) cvt_group(p, lds, group, t_lo, t_hi, bid, G);
;     else if (bid >= rem) cvt_group(p, lds, group, t_lo, t_hi, bid - rem, G - rem);
; }
.LBB0_919:
	s_or_b64 exec, exec, s[0:1]
	s_add_i32 s0, 0, 0x123e4
	v_mov_b32_e32 v2, s0
	s_waitcnt lgkmcnt(0)
	s_barrier
	ds_read_b32 v2, v2
	s_sub_i32 s31, s23, s4
	s_mul_i32 s0, s31, 6
	s_sub_i32 s0, 0x960, s0
	s_max_i32 s0, s0, 0
	s_lshr_b32 s0, s0, 8
	s_cmpk_lg_i32 s23, 0x100
	s_cselect_b32 s0, 0, s0
	s_mul_i32 s0, s0, s4
	s_sub_i32 s1, 0x960, s0
	s_sub_i32 s27, s98, s4
	s_nop 0
	s_add_i32 s0, s1, s98
	s_cmp_lt_i32 s98, s4
	s_cselect_b32 s27, s0, s27
	s_cselect_b32 s31, s4, s31
	s_cselect_b32 s1, 0x960, s1
	s_waitcnt lgkmcnt(0)
	v_lshlrev_b32_e32 v3, 6, v2
	v_add_u32_e32 v3, 0, v3
	v_add_u32_e32 v3, 0x12024, v3
	ds_read_b32 v3, v3
	v_readfirstlane_b32 s30, v2
	s_waitcnt lgkmcnt(0)
	v_min_i32_e32 v17, s1, v3
	v_cmp_ge_i32_e32 vcc, s27, v17
	s_cbranch_vccnz .LBB0_937
	s_cmp_gt_i32 s30, 1
	s_cselect_b64 s[0:1], -1, 0
	s_add_i32 s4, s30, -1
	s_cmp_lg_u32 s30, 2
	v_cndmask_b32_e64 v2, 0, 1, s[0:1]
	s_cselect_b64 s[0:1], -1, 0
	s_and_b32 s34, s4, -2
	s_or_b32 s35, s4, 1
	s_cmp_lg_u32 s4, s34
	v_cndmask_b32_e64 v4, 0, 1, s[0:1]
	s_cselect_b64 s[8:9], -1, 0
	v_cmp_ne_u32_e64 s[4:5], 1, v2
	s_add_i32 s40, 0, 0x120a4
	s_brev_b32 s41, 1
	v_lshlrev_b32_e32 v2, 2, v10
	v_mov_b32_e32 v3, 0
	v_add_u32_e32 v18, v15, v14
	s_movk_i32 s54, 0x4ff
	s_movk_i32 s55, 0xffcf
	s_mov_b32 s58, 0xc3e00000
	v_cmp_ne_u32_e64 s[6:7], 1, v4
	v_mov_b32_e32 v19, 0x43e00000
	s_branch .LBB0_923

; #define LAS __attribute__((address_space(3)))
; DI void cvt_group(const Params& p, LAS unsigned char* lds, int group, int t_lo, int t_hi, int r, int I) {
;     ...
;     __syncthreads();
;     const int nj = J[15].tile0, total = J[nj].tile0;
;     const int hi = min(t_hi, total);
;     const int row = tid >> 6, c4 = (tid & 63) * 4;
;     for (int gt = t_lo + r; gt < hi; gt += I) {
; DI void bg_range(const Params& p, LAS unsigned char* lds, int group, int t_lo, int t_hi, int nunits, int G, int bid) {
;     const int rem = nunits % G;
;     if (rem == 0) cvt_group(p, lds, group, t_lo, t_hi, bid, G);
;     else if (bid >= rem) cvt_group(p, lds, group, t_lo, t_hi, bid - rem, G - rem);
; }
.LBB0_1644:
	s_or_b64 exec, exec, s[0:1]
	s_add_i32 s0, 0, 0x123e4
	v_mov_b32_e32 v2, s0
	s_waitcnt lgkmcnt(0)
	s_barrier
	ds_read_b32 v2, v2
	s_sub_i32 s26, s23, s4
	s_mul_i32 s0, s26, 6
	s_sub_i32 s0, 0x800, s0
	s_max_i32 s0, s0, 0
	s_lshr_b32 s0, s0, 8
	s_cmpk_lg_i32 s23, 0x100
	s_cselect_b32 s0, 0, s0
	s_mul_i32 s0, s0, s4
	s_sub_i32 s1, 0x1800, s0
	s_sub_i32 s18, s98, s4
	s_add_i32 s18, s18, 0x1000
	s_add_i32 s0, s1, s98
	s_cmp_lt_i32 s98, s4
	s_cselect_b32 s18, s0, s18
	s_cselect_b32 s26, s4, s26
	s_cselect_b32 s1, 0x1800, s1
	s_waitcnt lgkmcnt(0)
	v_lshlrev_b32_e32 v3, 6, v2
	v_add_u32_e32 v3, 0, v3
	v_add_u32_e32 v3, 0x12024, v3
	ds_read_b32 v3, v3
	v_readfirstlane_b32 s19, v2
	s_waitcnt lgkmcnt(0)
	v_min_i32_e32 v17, s1, v3
	v_cmp_ge_i32_e32 vcc, s18, v17
	s_cbranch_vccnz .LBB0_1662
	s_cmp_gt_i32 s19, 1
	s_cselect_b64 s[0:1], -1, 0
	s_add_i32 s4, s19, -1
	s_cmp_lg_u32 s19, 2
	v_cndmask_b32_e64 v2, 0, 1, s[0:1]
	s_cselect_b64 s[0:1], -1, 0
	s_and_b32 s27, s4, -2
	s_or_b32 s30, s4, 1
	s_cmp_lg_u32 s4, s27
	v_cndmask_b32_e64 v4, 0, 1, s[0:1]
	s_cselect_b64 s[8:9], -1, 0
	v_cmp_ne_u32_e64 s[4:5], 1, v2
	s_add_i32 s31, 0, 0x120a4
	s_brev_b32 s34, 1
	v_lshlrev_b32_e32 v2, 2, v10
	v_mov_b32_e32 v3, 0
	v_add_u32_e32 v18, v15, v14
	s_movk_i32 s35, 0x4ff
	s_movk_i32 s36, 0xffcf
	s_mov_b32 s37, 0xc3e00000
	v_cmp_ne_u32_e64 s[6:7], 1, v4
	v_mov_b32_e32 v19, 0x43e00000
	s_branch .LBB0_1648
